# v25probe
# baseline (speedup 1.0000x reference)
.LBB1_12:
	s_waitcnt vmcnt(8)
	s_waitcnt lgkmcnt(0)
	s_barrier
	v_mfma_f32_16x16x32_f16 v[128:131], v[148:151], v[166:169], v[128:131]
	v_mfma_f32_16x16x32_f16 v[128:131], v[152:155], v[174:177], v[128:131]
	v_mfma_f32_16x16x32_f16 v[120:123], v[160:163], v[174:177], v[120:123]
	v_mfma_f32_16x16x32_f16 v[120:123], v[156:159], v[166:169], v[120:123]
	v_mfma_f32_16x16x32_f16 v[104:107], v[156:159], v[170:173], v[104:107]
	v_mfma_f32_16x16x32_f16 v[104:107], v[160:163], v[178:181], v[104:107]
	v_mfma_f32_16x16x32_f16 v[112:115], v[152:155], v[178:181], v[112:115]
	v_mfma_f32_16x16x32_f16 v[112:115], v[148:151], v[170:173], v[112:115]
	v_mfma_f32_16x16x32_f16 v[96:99], v[148:151], v[182:185], v[96:99]
	v_mfma_f32_16x16x32_f16 v[96:99], v[152:155], v[190:193], v[96:99]
	v_mfma_f32_16x16x32_f16 v[88:91], v[160:163], v[190:193], v[88:91]
	v_mfma_f32_16x16x32_f16 v[88:91], v[156:159], v[182:185], v[88:91]
	v_mfma_f32_16x16x32_f16 v[72:75], v[156:159], v[186:189], v[72:75]
	v_mfma_f32_16x16x32_f16 v[72:75], v[160:163], v[214:217], v[72:75]
	v_mfma_f32_16x16x32_f16 v[80:83], v[152:155], v[214:217], v[80:83]
	v_mfma_f32_16x16x32_f16 v[80:83], v[148:151], v[186:189], v[80:83]
	v_mfma_f32_16x16x32_f16 v[124:127], v[132:135], v[166:169], v[124:127]
	v_mfma_f32_16x16x32_f16 v[124:127], v[136:139], v[174:177], v[124:127]
	v_mfma_f32_16x16x32_f16 v[116:119], v[144:147], v[174:177], v[116:119]
	v_mfma_f32_16x16x32_f16 v[116:119], v[140:143], v[166:169], v[116:119]
	v_mfma_f32_16x16x32_f16 v[100:103], v[140:143], v[170:173], v[100:103]
	v_mfma_f32_16x16x32_f16 v[100:103], v[144:147], v[178:181], v[100:103]
	v_mfma_f32_16x16x32_f16 v[108:111], v[136:139], v[178:181], v[108:111]
	v_mfma_f32_16x16x32_f16 v[108:111], v[132:135], v[170:173], v[108:111]
	v_mfma_f32_16x16x32_f16 v[92:95], v[132:135], v[182:185], v[92:95]
	v_mfma_f32_16x16x32_f16 v[92:95], v[136:139], v[190:193], v[92:95]
	v_mfma_f32_16x16x32_f16 v[84:87], v[144:147], v[190:193], v[84:87]
	v_mfma_f32_16x16x32_f16 v[84:87], v[140:143], v[182:185], v[84:87]
	v_mfma_f32_16x16x32_f16 v[68:71], v[140:143], v[186:189], v[68:71]
	v_mfma_f32_16x16x32_f16 v[68:71], v[144:147], v[214:217], v[68:71]
	v_mfma_f32_16x16x32_f16 v[76:79], v[136:139], v[214:217], v[76:79]
	v_mfma_f32_16x16x32_f16 v[76:79], v[132:135], v[186:189], v[76:79]
	s_barrier
	s_sleep 1
	s_andn2_b64 vcc, exec, s[4:5]
	s_cbranch_vccnz .LBB1_16
	v_cvt_pkrtz_f16_f32 v166, v0, v1
	v_cvt_pkrtz_f16_f32 v167, v2, v3
	v_add_u32_e32 v166, 0x20002, v166
	v_add_u32_e32 v167, 0x20002, v167
	v_and_b32_e32 v166, 0xfffcfffc, v166
	v_and_b32_e32 v167, 0xfffcfffc, v167
	global_store_dwordx2 v231, v[166:167], s[90:91]

.LBB1_24:
	s_waitcnt lgkmcnt(0)
	s_barrier
	v_mfma_f32_16x16x32_f16 v[128:131], v[148:151], v[188:191], v[128:131]
	v_mfma_f32_16x16x32_f16 v[128:131], v[152:155], v[192:195], v[128:131]
	v_mfma_f32_16x16x32_f16 v[120:123], v[160:163], v[192:195], v[120:123]
	v_mfma_f32_16x16x32_f16 v[120:123], v[156:159], v[188:191], v[120:123]
	v_mfma_f32_16x16x32_f16 v[104:107], v[156:159], v[176:179], v[104:107]
	v_mfma_f32_16x16x32_f16 v[104:107], v[160:163], v[180:183], v[104:107]
	v_mfma_f32_16x16x32_f16 v[112:115], v[152:155], v[180:183], v[112:115]
	v_mfma_f32_16x16x32_f16 v[112:115], v[148:151], v[176:179], v[112:115]
	v_mfma_f32_16x16x32_f16 v[96:99], v[148:151], v[172:175], v[96:99]
	v_mfma_f32_16x16x32_f16 v[96:99], v[152:155], v[184:187], v[96:99]
	v_mfma_f32_16x16x32_f16 v[88:91], v[160:163], v[184:187], v[88:91]
	v_mfma_f32_16x16x32_f16 v[88:91], v[156:159], v[172:175], v[88:91]
	v_mfma_f32_16x16x32_f16 v[72:75], v[156:159], v[164:167], v[72:75]
	v_mfma_f32_16x16x32_f16 v[72:75], v[160:163], v[168:171], v[72:75]
	v_mfma_f32_16x16x32_f16 v[80:83], v[152:155], v[168:171], v[80:83]
	v_mfma_f32_16x16x32_f16 v[80:83], v[148:151], v[164:167], v[80:83]
	v_mfma_f32_16x16x32_f16 v[124:127], v[132:135], v[188:191], v[124:127]
	v_mfma_f32_16x16x32_f16 v[124:127], v[136:139], v[192:195], v[124:127]
	v_mfma_f32_16x16x32_f16 v[116:119], v[144:147], v[192:195], v[116:119]
	v_mfma_f32_16x16x32_f16 v[116:119], v[140:143], v[188:191], v[116:119]
	v_mfma_f32_16x16x32_f16 v[100:103], v[140:143], v[176:179], v[100:103]
	v_mfma_f32_16x16x32_f16 v[100:103], v[144:147], v[180:183], v[100:103]
	v_mfma_f32_16x16x32_f16 v[108:111], v[136:139], v[180:183], v[108:111]
	v_mfma_f32_16x16x32_f16 v[108:111], v[132:135], v[176:179], v[108:111]
	v_mfma_f32_16x16x32_f16 v[92:95], v[132:135], v[172:175], v[92:95]
	v_mfma_f32_16x16x32_f16 v[92:95], v[136:139], v[184:187], v[92:95]
	v_mfma_f32_16x16x32_f16 v[84:87], v[144:147], v[184:187], v[84:87]
	v_mfma_f32_16x16x32_f16 v[84:87], v[140:143], v[172:175], v[84:87]
	v_mfma_f32_16x16x32_f16 v[68:71], v[140:143], v[164:167], v[68:71]
	v_mfma_f32_16x16x32_f16 v[68:71], v[144:147], v[168:171], v[68:71]
	v_mfma_f32_16x16x32_f16 v[76:79], v[136:139], v[168:171], v[76:79]
	v_mfma_f32_16x16x32_f16 v[76:79], v[132:135], v[164:167], v[76:79]
	s_barrier
	s_sleep 1
	s_mov_b32 m0, s59
	s_add_u32 s4, s46, 0x100080
	ds_read_b128 v[164:167], v226 offset:49152
	ds_read_b128 v[168:171], v226 offset:51200
	ds_read_b128 v[172:175], v227 offset:49152
	ds_read_b128 v[176:179], v227 offset:51200
	ds_read_b128 v[180:183], v226 offset:53248
	ds_read_b128 v[184:187], v226 offset:55296
	ds_read_b128 v[188:191], v227 offset:53248
	ds_read_b128 v[192:195], v227 offset:55296
	global_load_lds_dwordx4 v200, s[84:85]
	s_mov_b32 m0, s60
	s_addc_u32 s5, s47, 0
	global_load_lds_dwordx4 v196, s[84:85]
	s_mov_b32 m0, s63
	s_nop 0
	global_load_lds_dwordx4 v200, s[4:5]
	s_mov_b32 m0, s64
	s_nop 0
	global_load_lds_dwordx4 v196, s[4:5]
	s_mov_b32 m0, s61
	s_nop 0
	global_load_lds_dwordx4 v202, s[86:87]
	s_mov_b32 m0, s62
	s_nop 0
	global_load_lds_dwordx4 v198, s[86:87]
	s_waitcnt vmcnt(8)
	s_waitcnt lgkmcnt(0)
	s_barrier
	v_mfma_f32_16x16x32_f16 v[64:67], v[148:151], v[164:167], v[64:67]
	v_mfma_f32_16x16x32_f16 v[64:67], v[152:155], v[172:175], v[64:67]
	v_mfma_f32_16x16x32_f16 v[56:59], v[160:163], v[172:175], v[56:59]
	v_mfma_f32_16x16x32_f16 v[56:59], v[156:159], v[164:167], v[56:59]
	v_mfma_f32_16x16x32_f16 v[40:43], v[156:159], v[168:171], v[40:43]
	v_mfma_f32_16x16x32_f16 v[40:43], v[160:163], v[176:179], v[40:43]
	v_mfma_f32_16x16x32_f16 v[48:51], v[152:155], v[176:179], v[48:51]
	v_mfma_f32_16x16x32_f16 v[48:51], v[148:151], v[168:171], v[48:51]
	v_mfma_f32_16x16x32_f16 v[32:35], v[148:151], v[180:183], v[32:35]
	v_mfma_f32_16x16x32_f16 v[32:35], v[152:155], v[188:191], v[32:35]
	v_mfma_f32_16x16x32_f16 v[24:27], v[160:163], v[188:191], v[24:27]
	v_mfma_f32_16x16x32_f16 v[24:27], v[156:159], v[180:183], v[24:27]
	v_mfma_f32_16x16x32_f16 v[8:11], v[156:159], v[184:187], v[8:11]
	v_mfma_f32_16x16x32_f16 v[8:11], v[160:163], v[192:195], v[8:11]
	v_mfma_f32_16x16x32_f16 v[16:19], v[152:155], v[192:195], v[16:19]
	v_mfma_f32_16x16x32_f16 v[16:19], v[148:151], v[184:187], v[16:19]
	v_mfma_f32_16x16x32_f16 v[60:63], v[132:135], v[164:167], v[60:63]
	v_mfma_f32_16x16x32_f16 v[60:63], v[136:139], v[172:175], v[60:63]
	v_mfma_f32_16x16x32_f16 v[52:55], v[144:147], v[172:175], v[52:55]
	v_mfma_f32_16x16x32_f16 v[52:55], v[140:143], v[164:167], v[52:55]
	v_mfma_f32_16x16x32_f16 v[36:39], v[140:143], v[168:171], v[36:39]
	v_mfma_f32_16x16x32_f16 v[36:39], v[144:147], v[176:179], v[36:39]
	v_mfma_f32_16x16x32_f16 v[44:47], v[136:139], v[176:179], v[44:47]
	v_mfma_f32_16x16x32_f16 v[44:47], v[132:135], v[168:171], v[44:47]
	v_mfma_f32_16x16x32_f16 v[28:31], v[132:135], v[180:183], v[28:31]
	v_mfma_f32_16x16x32_f16 v[28:31], v[136:139], v[188:191], v[28:31]
	v_mfma_f32_16x16x32_f16 v[20:23], v[144:147], v[188:191], v[20:23]
	v_mfma_f32_16x16x32_f16 v[20:23], v[140:143], v[180:183], v[20:23]
	v_mfma_f32_16x16x32_f16 v[4:7], v[140:143], v[184:187], v[4:7]
	v_mfma_f32_16x16x32_f16 v[4:7], v[144:147], v[192:195], v[4:7]
	v_mfma_f32_16x16x32_f16 v[12:15], v[136:139], v[192:195], v[12:15]
	v_mfma_f32_16x16x32_f16 v[12:15], v[132:135], v[184:187], v[12:15]
	s_barrier
	s_add_u32 s80, s80, 0x100
	s_addc_u32 s81, s81, 0
	s_add_u32 s44, s44, 0x100
	s_addc_u32 s45, s45, 0
	s_cmp_gt_u32 s82, 61
	s_cbranch_scc1 .LBB1_4
	s_mov_b32 s48, s82
	s_branch .LBB1_9

.LBB1_30:
	s_endpgm
	s_nop 0
	s_endpgm

.LBB2_20:
	s_add_u32 s30, s28, 0xffc80080
	s_addc_u32 s31, s29, -1
	s_cmpk_eq_i32 s58, 0xdc
	s_cselect_b32 s35, s25, s31
	s_cselect_b32 s34, s24, s30
	s_cselect_b32 s31, s27, s57
	s_cselect_b32 s30, s26, s56
	s_add_i32 m0, s37, 0xc000
	ds_read_b128 v[166:169], v143
	ds_read_b128 v[170:173], v147
	ds_read_b128 v[174:177], v149
	ds_read_b128 v[178:181], v150
	ds_read_b128 v[182:185], v151
	ds_read_b128 v[186:189], v152
	ds_read_b128 v[190:193], v153
	ds_read_b128 v[194:197], v154
	ds_read_b128 v[198:201], v155
	ds_read_b128 v[202:205], v155 offset:2048
	ds_read_b128 v[206:209], v156
	ds_read_b128 v[210:213], v156 offset:2048
	ds_read_b128 v[214:217], v155 offset:4096
	ds_read_b128 v[218:221], v155 offset:6144
	ds_read_b128 v[222:225], v156 offset:4096
	ds_read_b128 v[226:229], v156 offset:6144
	global_load_lds_dwordx4 v134, s[28:29]
	s_add_i32 m0, s37, 0xe000
	s_nop 0
	global_load_lds_dwordx4 v132, s[28:29]
	s_waitcnt vmcnt(8)
	s_waitcnt lgkmcnt(0)
	s_barrier
	v_mfma_f32_16x16x32_f16 v[124:127], v[166:169], v[198:201], v[124:127]
	v_mfma_f32_16x16x32_f16 v[124:127], v[170:173], v[206:209], v[124:127]
	v_mfma_f32_16x16x32_f16 v[120:123], v[178:181], v[206:209], v[120:123]
	v_mfma_f32_16x16x32_f16 v[120:123], v[174:177], v[198:201], v[120:123]
	v_mfma_f32_16x16x32_f16 v[112:115], v[174:177], v[202:205], v[112:115]
	v_mfma_f32_16x16x32_f16 v[112:115], v[178:181], v[210:213], v[112:115]
	v_mfma_f32_16x16x32_f16 v[116:119], v[170:173], v[210:213], v[116:119]
	v_mfma_f32_16x16x32_f16 v[116:119], v[166:169], v[202:205], v[116:119]
	v_mfma_f32_16x16x32_f16 v[108:111], v[166:169], v[214:217], v[108:111]
	v_mfma_f32_16x16x32_f16 v[108:111], v[170:173], v[222:225], v[108:111]
	v_mfma_f32_16x16x32_f16 v[100:103], v[178:181], v[222:225], v[100:103]
	v_mfma_f32_16x16x32_f16 v[100:103], v[174:177], v[214:217], v[100:103]
	v_mfma_f32_16x16x32_f16 v[84:87], v[174:177], v[218:221], v[84:87]
	v_mfma_f32_16x16x32_f16 v[84:87], v[178:181], v[226:229], v[84:87]
	v_mfma_f32_16x16x32_f16 v[92:95], v[170:173], v[226:229], v[92:95]
	v_mfma_f32_16x16x32_f16 v[92:95], v[166:169], v[218:221], v[92:95]
	v_mfma_f32_16x16x32_f16 v[104:107], v[182:185], v[198:201], v[104:107]
	v_mfma_f32_16x16x32_f16 v[104:107], v[186:189], v[206:209], v[104:107]
	v_mfma_f32_16x16x32_f16 v[96:99], v[194:197], v[206:209], v[96:99]
	v_mfma_f32_16x16x32_f16 v[96:99], v[190:193], v[198:201], v[96:99]
	v_mfma_f32_16x16x32_f16 v[80:83], v[190:193], v[202:205], v[80:83]
	v_mfma_f32_16x16x32_f16 v[80:83], v[194:197], v[210:213], v[80:83]
	v_mfma_f32_16x16x32_f16 v[88:91], v[186:189], v[210:213], v[88:91]
	v_mfma_f32_16x16x32_f16 v[88:91], v[182:185], v[202:205], v[88:91]
	v_mfma_f32_16x16x32_f16 v[76:79], v[182:185], v[214:217], v[76:79]
	v_mfma_f32_16x16x32_f16 v[76:79], v[186:189], v[222:225], v[76:79]
	v_mfma_f32_16x16x32_f16 v[72:75], v[194:197], v[222:225], v[72:75]
	v_mfma_f32_16x16x32_f16 v[72:75], v[190:193], v[214:217], v[72:75]
	v_mfma_f32_16x16x32_f16 v[64:67], v[190:193], v[218:221], v[64:67]
	v_mfma_f32_16x16x32_f16 v[64:67], v[194:197], v[226:229], v[64:67]
	v_mfma_f32_16x16x32_f16 v[68:71], v[186:189], v[226:229], v[68:71]
	v_mfma_f32_16x16x32_f16 v[68:71], v[182:185], v[218:221], v[68:71]
	s_barrier
	s_sleep 1
	s_add_i32 s59, s43, s36
	s_mov_b32 m0, s59
	ds_read_b128 v[198:201], v155 offset:16384
	ds_read_b128 v[202:205], v155 offset:18432
	ds_read_b128 v[206:209], v156 offset:16384
	ds_read_b128 v[210:213], v156 offset:18432
	ds_read_b128 v[214:217], v155 offset:20480
	ds_read_b128 v[218:221], v155 offset:22528
	ds_read_b128 v[222:225], v156 offset:20480
	ds_read_b128 v[226:229], v156 offset:22528
	global_load_lds_dwordx4 v128, s[30:31]
	s_add_i32 m0, s59, 0x2000
	s_add_u32 s60, s30, 0x380000
	s_addc_u32 s61, s31, 0
	s_add_i32 s59, s44, s36
	global_load_lds_dwordx4 v130, s[30:31]
	s_mov_b32 m0, s59
	s_add_u32 s62, s30, 0x80
	s_addc_u32 s63, s31, 0
	global_load_lds_dwordx4 v128, s[60:61]
	s_add_i32 m0, s59, 0x2000
	s_add_u32 s64, s34, 0x80
	s_addc_u32 s65, s35, 0
	global_load_lds_dwordx4 v130, s[60:61]
	s_mov_b32 m0, s37
	s_nop 0
	global_load_lds_dwordx4 v128, s[34:35]
	s_mov_b32 m0, s38
	s_nop 0
	global_load_lds_dwordx4 v130, s[34:35]
	s_waitcnt vmcnt(8)
	s_waitcnt lgkmcnt(0)
	s_barrier
	v_mfma_f32_16x16x32_f16 v[60:63], v[166:169], v[198:201], v[60:63]
	v_mfma_f32_16x16x32_f16 v[60:63], v[170:173], v[206:209], v[60:63]
	v_mfma_f32_16x16x32_f16 v[56:59], v[178:181], v[206:209], v[56:59]
	v_mfma_f32_16x16x32_f16 v[56:59], v[174:177], v[198:201], v[56:59]
	v_mfma_f32_16x16x32_f16 v[48:51], v[174:177], v[202:205], v[48:51]
	v_mfma_f32_16x16x32_f16 v[48:51], v[178:181], v[210:213], v[48:51]
	v_mfma_f32_16x16x32_f16 v[52:55], v[170:173], v[210:213], v[52:55]
	v_mfma_f32_16x16x32_f16 v[52:55], v[166:169], v[202:205], v[52:55]
	v_mfma_f32_16x16x32_f16 v[40:43], v[166:169], v[214:217], v[40:43]
	v_mfma_f32_16x16x32_f16 v[40:43], v[170:173], v[222:225], v[40:43]
	v_mfma_f32_16x16x32_f16 v[32:35], v[178:181], v[222:225], v[32:35]
	v_mfma_f32_16x16x32_f16 v[32:35], v[174:177], v[214:217], v[32:35]
	v_mfma_f32_16x16x32_f16 v[8:11], v[174:177], v[218:221], v[8:11]
	v_mfma_f32_16x16x32_f16 v[8:11], v[178:181], v[226:229], v[8:11]
	v_mfma_f32_16x16x32_f16 v[12:15], v[170:173], v[226:229], v[12:15]
	v_mfma_f32_16x16x32_f16 v[12:15], v[166:169], v[218:221], v[12:15]
	v_mfma_f32_16x16x32_f16 v[44:47], v[182:185], v[198:201], v[44:47]
	v_mfma_f32_16x16x32_f16 v[44:47], v[186:189], v[206:209], v[44:47]
	v_mfma_f32_16x16x32_f16 v[36:39], v[194:197], v[206:209], v[36:39]
	v_mfma_f32_16x16x32_f16 v[36:39], v[190:193], v[198:201], v[36:39]
	v_mfma_f32_16x16x32_f16 v[24:27], v[190:193], v[202:205], v[24:27]
	v_mfma_f32_16x16x32_f16 v[24:27], v[194:197], v[210:213], v[24:27]
	v_mfma_f32_16x16x32_f16 v[28:31], v[186:189], v[210:213], v[28:31]
	v_mfma_f32_16x16x32_f16 v[28:31], v[182:185], v[202:205], v[28:31]
	v_mfma_f32_16x16x32_f16 v[20:23], v[182:185], v[214:217], v[20:23]
	v_mfma_f32_16x16x32_f16 v[20:23], v[186:189], v[222:225], v[20:23]
	v_mfma_f32_16x16x32_f16 v[16:19], v[194:197], v[222:225], v[16:19]
	v_mfma_f32_16x16x32_f16 v[16:19], v[190:193], v[214:217], v[16:19]
	v_mfma_f32_16x16x32_f16 v[0:3], v[190:193], v[218:221], v[0:3]
	v_mfma_f32_16x16x32_f16 v[0:3], v[194:197], v[226:229], v[0:3]
	v_mfma_f32_16x16x32_f16 v[4:7], v[186:189], v[226:229], v[4:7]
	v_mfma_f32_16x16x32_f16 v[4:7], v[182:185], v[218:221], v[4:7]
	s_barrier
	s_add_u32 s34, s34, 0x380000
	s_addc_u32 s35, s35, 0
	s_mov_b32 m0, s39
	ds_read_b128 v[166:169], v157
	ds_read_b128 v[170:173], v158
	ds_read_b128 v[174:177], v159
	ds_read_b128 v[178:181], v160
	ds_read_b128 v[182:185], v161
	ds_read_b128 v[186:189], v162
	ds_read_b128 v[190:193], v163
	ds_read_b128 v[194:197], v164
	ds_read_b128 v[198:201], v155 offset:32768
	ds_read_b128 v[202:205], v155 offset:34816
	ds_read_b128 v[206:209], v156 offset:32768
	ds_read_b128 v[210:213], v156 offset:34816
	ds_read_b128 v[214:217], v155 offset:36864
	ds_read_b128 v[218:221], v155 offset:38912
	ds_read_b128 v[222:225], v156 offset:36864
	ds_read_b128 v[226:229], v156 offset:38912
	global_load_lds_dwordx4 v128, s[34:35]
	s_mov_b32 m0, s40
	s_nop 0
	global_load_lds_dwordx4 v130, s[34:35]
	s_waitcnt vmcnt(8)
	s_waitcnt lgkmcnt(0)
	s_barrier
	v_mfma_f32_16x16x32_f16 v[124:127], v[166:169], v[198:201], v[124:127]
	v_mfma_f32_16x16x32_f16 v[124:127], v[170:173], v[206:209], v[124:127]
	v_mfma_f32_16x16x32_f16 v[120:123], v[178:181], v[206:209], v[120:123]
	v_mfma_f32_16x16x32_f16 v[120:123], v[174:177], v[198:201], v[120:123]
	v_mfma_f32_16x16x32_f16 v[112:115], v[174:177], v[202:205], v[112:115]
	v_mfma_f32_16x16x32_f16 v[112:115], v[178:181], v[210:213], v[112:115]
	v_mfma_f32_16x16x32_f16 v[116:119], v[170:173], v[210:213], v[116:119]
	v_mfma_f32_16x16x32_f16 v[116:119], v[166:169], v[202:205], v[116:119]
	v_mfma_f32_16x16x32_f16 v[108:111], v[166:169], v[214:217], v[108:111]
	v_mfma_f32_16x16x32_f16 v[108:111], v[170:173], v[222:225], v[108:111]
	v_mfma_f32_16x16x32_f16 v[100:103], v[178:181], v[222:225], v[100:103]
	v_mfma_f32_16x16x32_f16 v[100:103], v[174:177], v[214:217], v[100:103]
	v_mfma_f32_16x16x32_f16 v[84:87], v[174:177], v[218:221], v[84:87]
	v_mfma_f32_16x16x32_f16 v[84:87], v[178:181], v[226:229], v[84:87]
	v_mfma_f32_16x16x32_f16 v[92:95], v[170:173], v[226:229], v[92:95]
	v_mfma_f32_16x16x32_f16 v[92:95], v[166:169], v[218:221], v[92:95]
	v_mfma_f32_16x16x32_f16 v[104:107], v[182:185], v[198:201], v[104:107]
	v_mfma_f32_16x16x32_f16 v[104:107], v[186:189], v[206:209], v[104:107]
	v_mfma_f32_16x16x32_f16 v[96:99], v[194:197], v[206:209], v[96:99]
	v_mfma_f32_16x16x32_f16 v[96:99], v[190:193], v[198:201], v[96:99]
	v_mfma_f32_16x16x32_f16 v[80:83], v[190:193], v[202:205], v[80:83]
	v_mfma_f32_16x16x32_f16 v[80:83], v[194:197], v[210:213], v[80:83]
	v_mfma_f32_16x16x32_f16 v[88:91], v[186:189], v[210:213], v[88:91]
	v_mfma_f32_16x16x32_f16 v[88:91], v[182:185], v[202:205], v[88:91]
	v_mfma_f32_16x16x32_f16 v[76:79], v[182:185], v[214:217], v[76:79]
	v_mfma_f32_16x16x32_f16 v[76:79], v[186:189], v[222:225], v[76:79]
	v_mfma_f32_16x16x32_f16 v[72:75], v[194:197], v[222:225], v[72:75]
	v_mfma_f32_16x16x32_f16 v[72:75], v[190:193], v[214:217], v[72:75]
	v_mfma_f32_16x16x32_f16 v[64:67], v[190:193], v[218:221], v[64:67]
	v_mfma_f32_16x16x32_f16 v[64:67], v[194:197], v[226:229], v[64:67]
	v_mfma_f32_16x16x32_f16 v[68:71], v[186:189], v[226:229], v[68:71]
	v_mfma_f32_16x16x32_f16 v[68:71], v[182:185], v[218:221], v[68:71]
	s_barrier
	s_sleep 1
	s_add_i32 s34, s46, s36
	s_mov_b32 m0, s34
	ds_read_b128 v[198:201], v155 offset:49152
	ds_read_b128 v[202:205], v155 offset:51200
	ds_read_b128 v[206:209], v156 offset:49152
	ds_read_b128 v[210:213], v156 offset:51200
	ds_read_b128 v[214:217], v155 offset:53248
	ds_read_b128 v[218:221], v155 offset:55296
	ds_read_b128 v[222:225], v156 offset:53248
	ds_read_b128 v[226:229], v156 offset:55296
	global_load_lds_dwordx4 v128, s[62:63]
	s_add_i32 m0, s34, 0x2000
	s_add_u32 s30, s30, 0x380080
	s_addc_u32 s31, s31, 0
	s_add_i32 s34, s47, s36
	global_load_lds_dwordx4 v130, s[62:63]
	s_mov_b32 m0, s34
	s_nop 0
	global_load_lds_dwordx4 v128, s[30:31]
	s_add_i32 m0, s34, 0x2000
	s_nop 0
	global_load_lds_dwordx4 v130, s[30:31]
	s_mov_b32 m0, s41
	s_nop 0
	global_load_lds_dwordx4 v128, s[64:65]
	s_mov_b32 m0, s42
	s_nop 0
	global_load_lds_dwordx4 v130, s[64:65]
	s_waitcnt vmcnt(8)
	s_waitcnt lgkmcnt(0)
	s_barrier
	v_mfma_f32_16x16x32_f16 v[60:63], v[166:169], v[198:201], v[60:63]
	v_mfma_f32_16x16x32_f16 v[60:63], v[170:173], v[206:209], v[60:63]
	v_mfma_f32_16x16x32_f16 v[56:59], v[178:181], v[206:209], v[56:59]
	v_mfma_f32_16x16x32_f16 v[56:59], v[174:177], v[198:201], v[56:59]
	v_mfma_f32_16x16x32_f16 v[48:51], v[174:177], v[202:205], v[48:51]
	v_mfma_f32_16x16x32_f16 v[48:51], v[178:181], v[210:213], v[48:51]
	v_mfma_f32_16x16x32_f16 v[52:55], v[170:173], v[210:213], v[52:55]
	v_mfma_f32_16x16x32_f16 v[52:55], v[166:169], v[202:205], v[52:55]
	v_mfma_f32_16x16x32_f16 v[40:43], v[166:169], v[214:217], v[40:43]
	v_mfma_f32_16x16x32_f16 v[40:43], v[170:173], v[222:225], v[40:43]
	v_mfma_f32_16x16x32_f16 v[32:35], v[178:181], v[222:225], v[32:35]
	v_mfma_f32_16x16x32_f16 v[32:35], v[174:177], v[214:217], v[32:35]
	v_mfma_f32_16x16x32_f16 v[8:11], v[174:177], v[218:221], v[8:11]
	v_mfma_f32_16x16x32_f16 v[8:11], v[178:181], v[226:229], v[8:11]
	v_mfma_f32_16x16x32_f16 v[12:15], v[170:173], v[226:229], v[12:15]
	v_mfma_f32_16x16x32_f16 v[12:15], v[166:169], v[218:221], v[12:15]
	v_mfma_f32_16x16x32_f16 v[44:47], v[182:185], v[198:201], v[44:47]
	v_mfma_f32_16x16x32_f16 v[44:47], v[186:189], v[206:209], v[44:47]
	v_mfma_f32_16x16x32_f16 v[36:39], v[194:197], v[206:209], v[36:39]
	v_mfma_f32_16x16x32_f16 v[36:39], v[190:193], v[198:201], v[36:39]
	v_mfma_f32_16x16x32_f16 v[24:27], v[190:193], v[202:205], v[24:27]
	v_mfma_f32_16x16x32_f16 v[24:27], v[194:197], v[210:213], v[24:27]
	v_mfma_f32_16x16x32_f16 v[28:31], v[186:189], v[210:213], v[28:31]
	v_mfma_f32_16x16x32_f16 v[28:31], v[182:185], v[202:205], v[28:31]
	v_mfma_f32_16x16x32_f16 v[20:23], v[182:185], v[214:217], v[20:23]
	v_mfma_f32_16x16x32_f16 v[20:23], v[186:189], v[222:225], v[20:23]
	v_mfma_f32_16x16x32_f16 v[16:19], v[194:197], v[222:225], v[16:19]
	v_mfma_f32_16x16x32_f16 v[16:19], v[190:193], v[214:217], v[16:19]
	v_mfma_f32_16x16x32_f16 v[0:3], v[190:193], v[218:221], v[0:3]
	v_mfma_f32_16x16x32_f16 v[0:3], v[194:197], v[226:229], v[0:3]
	v_mfma_f32_16x16x32_f16 v[4:7], v[186:189], v[226:229], v[4:7]
	v_mfma_f32_16x16x32_f16 v[4:7], v[182:185], v[218:221], v[4:7]
	s_barrier
	s_add_i32 s58, s58, 2
	s_add_u32 s56, s56, 0x100
	s_addc_u32 s57, s57, 0
	s_add_u32 s28, s28, 0x100
	s_addc_u32 s29, s29, 0
	s_cmpk_gt_u32 s58, 0xdd
	s_cbranch_scc0 .LBB2_20
	v_lshl_add_u32 v144, s55, 8, v137
	v_ashrrev_i32_e32 v145, 31, v144
	v_lshl_add_u64 v[138:139], v[144:145], 2, s[10:11]
	global_load_dword v136, v[138:139], off
	global_load_dword v140, v[138:139], off offset:64
	global_load_dword v142, v[138:139], off offset:128
	global_load_dword v146, v[138:139], off offset:192
	global_load_dword v148, v[138:139], off offset:512
	global_load_dword v174, v[138:139], off offset:576
	global_load_dword v176, v[138:139], off offset:640
	s_nop 0
	global_load_dword v138, v[138:139], off offset:704
	v_lshl_or_b32 v166, s54, 8, v141
	v_ashrrev_i32_e32 v167, 31, v166
	v_or_b32_e32 v168, 16, v144
	v_or_b32_e32 v170, 32, v144
	v_or_b32_e32 v172, 48, v144
	v_lshl_add_u64 v[166:167], v[166:167], 2, s[8:9]
	v_lshlrev_b64 v[144:145], 14, v[144:145]
	v_ashrrev_i32_e32 v169, 31, v168
	v_ashrrev_i32_e32 v171, 31, v170
	v_ashrrev_i32_e32 v173, 31, v172
	v_lshl_add_u64 v[144:145], v[166:167], 0, v[144:145]
	v_lshlrev_b64 v[168:169], 14, v[168:169]
	v_lshlrev_b64 v[170:171], 14, v[170:171]
	v_lshlrev_b64 v[172:173], 14, v[172:173]
	v_add_co_u32_e32 v178, vcc, s48, v144
	v_lshl_add_u64 v[168:169], v[166:167], 0, v[168:169]
	v_lshl_add_u64 v[170:171], v[166:167], 0, v[170:171]
	v_lshl_add_u64 v[166:167], v[166:167], 0, v[172:173]
	v_lshl_add_u64 v[172:173], v[144:145], 0, s[16:17]
	v_addc_co_u32_e32 v179, vcc, 0, v145, vcc
	s_mov_b32 s55, s45
	s_mov_b32 s54, s53
	s_mov_b64 s[28:29], s[26:27]
	s_mov_b64 s[30:31], s[24:25]
	s_waitcnt vmcnt(0)
	v_pk_mul_f32 v[126:127], v[136:137], v[126:127] op_sel_hi:[0,1]
	v_pk_mul_f32 v[124:125], v[136:137], v[124:125] op_sel_hi:[0,1]
	v_pk_mul_f32 v[122:123], v[136:137], v[122:123] op_sel_hi:[0,1]
	v_pk_mul_f32 v[120:121], v[136:137], v[120:121] op_sel_hi:[0,1]
	v_pk_mul_f32 v[46:47], v[148:149], v[46:47] op_sel_hi:[0,1]
	v_pk_mul_f32 v[44:45], v[148:149], v[44:45] op_sel_hi:[0,1]
	v_pk_mul_f32 v[106:107], v[136:137], v[106:107] op_sel_hi:[0,1]
	v_pk_mul_f32 v[104:105], v[136:137], v[104:105] op_sel_hi:[0,1]
	v_pk_mul_f32 v[98:99], v[136:137], v[98:99] op_sel_hi:[0,1]
	v_pk_mul_f32 v[96:97], v[136:137], v[96:97] op_sel_hi:[0,1]
	v_pk_mul_f32 v[118:119], v[140:141], v[118:119] op_sel_hi:[0,1]
	v_pk_mul_f32 v[116:117], v[140:141], v[116:117] op_sel_hi:[0,1]
	v_pk_mul_f32 v[114:115], v[140:141], v[114:115] op_sel_hi:[0,1]
	v_pk_mul_f32 v[112:113], v[140:141], v[112:113] op_sel_hi:[0,1]
	v_pk_mul_f32 v[90:91], v[140:141], v[90:91] op_sel_hi:[0,1]
	v_pk_mul_f32 v[88:89], v[140:141], v[88:89] op_sel_hi:[0,1]
	v_pk_mul_f32 v[82:83], v[140:141], v[82:83] op_sel_hi:[0,1]
	v_pk_mul_f32 v[80:81], v[140:141], v[80:81] op_sel_hi:[0,1]
	v_pk_mul_f32 v[110:111], v[142:143], v[110:111] op_sel_hi:[0,1]
	v_pk_mul_f32 v[108:109], v[142:143], v[108:109] op_sel_hi:[0,1]
	v_pk_mul_f32 v[102:103], v[142:143], v[102:103] op_sel_hi:[0,1]
	v_pk_mul_f32 v[100:101], v[142:143], v[100:101] op_sel_hi:[0,1]
	v_pk_mul_f32 v[78:79], v[142:143], v[78:79] op_sel_hi:[0,1]
	v_pk_mul_f32 v[76:77], v[142:143], v[76:77] op_sel_hi:[0,1]
	v_pk_mul_f32 v[74:75], v[142:143], v[74:75] op_sel_hi:[0,1]
	v_pk_mul_f32 v[72:73], v[142:143], v[72:73] op_sel_hi:[0,1]
	v_pk_mul_f32 v[94:95], v[146:147], v[94:95] op_sel_hi:[0,1]
	v_pk_mul_f32 v[92:93], v[146:147], v[92:93] op_sel_hi:[0,1]
	v_pk_mul_f32 v[86:87], v[146:147], v[86:87] op_sel_hi:[0,1]
	v_pk_mul_f32 v[84:85], v[146:147], v[84:85] op_sel_hi:[0,1]
	v_pk_mul_f32 v[70:71], v[146:147], v[70:71] op_sel_hi:[0,1]
	v_pk_mul_f32 v[68:69], v[146:147], v[68:69] op_sel_hi:[0,1]
	v_pk_mul_f32 v[66:67], v[146:147], v[66:67] op_sel_hi:[0,1]
	v_pk_mul_f32 v[64:65], v[146:147], v[64:65] op_sel_hi:[0,1]
	v_pk_mul_f32 v[62:63], v[148:149], v[62:63] op_sel_hi:[0,1]
	v_pk_mul_f32 v[60:61], v[148:149], v[60:61] op_sel_hi:[0,1]
	global_store_dwordx4 v[144:145], v[124:127], off
	global_store_dwordx4 v[144:145], v[120:123], off offset:64
	global_store_dwordx4 v[144:145], v[104:107], off offset:512
	global_store_dwordx4 v[144:145], v[96:99], off offset:576
	global_store_dwordx4 v[168:169], v[116:119], off
	global_store_dwordx4 v[168:169], v[112:115], off offset:64
	global_store_dwordx4 v[168:169], v[88:91], off offset:512
	global_store_dwordx4 v[168:169], v[80:83], off offset:576
	global_store_dwordx4 v[170:171], v[108:111], off
	global_store_dwordx4 v[170:171], v[100:103], off offset:64
	global_store_dwordx4 v[170:171], v[76:79], off offset:512
	global_store_dwordx4 v[170:171], v[72:75], off offset:576
	global_store_dwordx4 v[166:167], v[92:95], off
	global_store_dwordx4 v[166:167], v[84:87], off offset:64
	global_store_dwordx4 v[166:167], v[68:71], off offset:512
	global_store_dwordx4 v[166:167], v[64:67], off offset:576
	global_store_dwordx4 v[178:179], v[60:63], off
	global_store_dwordx4 v[172:173], v[44:47], off offset:512
	v_pk_mul_f32 v[30:31], v[174:175], v[30:31] op_sel_hi:[0,1]
	v_pk_mul_f32 v[28:29], v[174:175], v[28:29] op_sel_hi:[0,1]
	v_add_co_u32_e32 v46, vcc, s49, v144
	v_lshl_add_u64 v[44:45], v[144:145], 0, s[18:19]
	s_nop 0
	v_addc_co_u32_e32 v47, vcc, 0, v145, vcc
	global_store_dwordx4 v[44:45], v[28:31], off offset:512
	v_pk_mul_f32 v[18:19], v[176:177], v[18:19] op_sel_hi:[0,1]
	v_pk_mul_f32 v[16:17], v[176:177], v[16:17] op_sel_hi:[0,1]
	v_add_co_u32_e32 v30, vcc, s50, v144
	v_lshl_add_u64 v[28:29], v[144:145], 0, s[20:21]
	s_nop 0
	v_addc_co_u32_e32 v31, vcc, 0, v145, vcc
	v_pk_mul_f32 v[38:39], v[148:149], v[38:39] op_sel_hi:[0,1]
	v_pk_mul_f32 v[36:37], v[148:149], v[36:37] op_sel_hi:[0,1]
	v_pk_mul_f32 v[26:27], v[174:175], v[26:27] op_sel_hi:[0,1]
	v_pk_mul_f32 v[24:25], v[174:175], v[24:25] op_sel_hi:[0,1]
	global_store_dwordx4 v[28:29], v[16:19], off offset:576
	global_store_dwordx4 v[172:173], v[36:39], off offset:576
	global_store_dwordx4 v[44:45], v[24:27], off offset:576
	v_add_co_u32_e32 v18, vcc, s51, v144
	v_pk_mul_f32 v[38:39], v[174:175], v[54:55] op_sel_hi:[0,1]
	v_pk_mul_f32 v[36:37], v[174:175], v[52:53] op_sel_hi:[0,1]
	v_pk_mul_f32 v[26:27], v[176:177], v[42:43] op_sel_hi:[0,1]
	v_pk_mul_f32 v[24:25], v[176:177], v[40:41] op_sel_hi:[0,1]
	v_addc_co_u32_e32 v19, vcc, 0, v145, vcc
	v_pk_mul_f32 v[58:59], v[148:149], v[58:59] op_sel_hi:[0,1]
	v_pk_mul_f32 v[56:57], v[148:149], v[56:57] op_sel_hi:[0,1]
	global_store_dwordx4 v[46:47], v[36:39], off
	global_store_dwordx4 v[30:31], v[24:27], off
	v_pk_mul_f32 v[22:23], v[176:177], v[22:23] op_sel_hi:[0,1]
	v_pk_mul_f32 v[38:39], v[174:175], v[50:51] op_sel_hi:[0,1]
	v_pk_mul_f32 v[36:37], v[174:175], v[48:49] op_sel_hi:[0,1]
	v_pk_mul_f32 v[26:27], v[176:177], v[34:35] op_sel_hi:[0,1]
	v_pk_mul_f32 v[24:25], v[176:177], v[32:33] op_sel_hi:[0,1]
	v_pk_mul_f32 v[20:21], v[176:177], v[20:21] op_sel_hi:[0,1]
	v_lshl_add_u64 v[16:17], v[144:145], 0, s[22:23]
	v_pk_mul_f32 v[14:15], v[138:139], v[14:15] op_sel_hi:[0,1]
	v_pk_mul_f32 v[12:13], v[138:139], v[12:13] op_sel_hi:[0,1]
	v_pk_mul_f32 v[10:11], v[138:139], v[10:11] op_sel_hi:[0,1]
	v_pk_mul_f32 v[8:9], v[138:139], v[8:9] op_sel_hi:[0,1]
	v_pk_mul_f32 v[6:7], v[138:139], v[6:7] op_sel_hi:[0,1]
	v_pk_mul_f32 v[4:5], v[138:139], v[4:5] op_sel_hi:[0,1]
	v_pk_mul_f32 v[2:3], v[138:139], v[2:3] op_sel_hi:[0,1]
	v_pk_mul_f32 v[0:1], v[138:139], v[0:1] op_sel_hi:[0,1]
	s_mov_b64 vcc, s[0:1]
	global_store_dwordx4 v[172:173], v[56:59], off offset:64
	global_store_dwordx4 v[44:45], v[36:39], off offset:64
	global_store_dwordx4 v[28:29], v[24:27], off offset:64
	global_store_dwordx4 v[28:29], v[20:23], off offset:512
	global_store_dwordx4 v[18:19], v[12:15], off
	global_store_dwordx4 v[16:17], v[8:11], off offset:64
	global_store_dwordx4 v[16:17], v[4:7], off offset:512
	global_store_dwordx4 v[16:17], v[0:3], off offset:576
	s_cbranch_vccz .LBB2_8
	s_waitcnt vmcnt(0)
	s_cmpk_gt_u32 s33, 0xff
	s_cbranch_scc1 .LBB2_24
	s_barrier
